# s17 + attention row-sum chains: the 13 in-place x+0 adds removed
# speedup vs baseline: 1.0013x; 1.0013x over previous
; template <bool MOBA, int THRL> ...
;     ...
;     if (MOBA && qb >= 4) {
;         float gate[8];
; #pragma unroll
;         for (int n = 0; n < 8; ++n) gate[n] = 0.f;
; #pragma unroll
;         for (int d0 = 0; d0 < 4; ++d0) {
;             const h16x8 qv = __builtin_bit_cast(h16x8, qr[d0]);
; #pragma unroll
;             for (int n = 0; n < 7; ++n) {
;                 const f32x4 k0 = *(lds_cf32x4*)(shm3 + LDS_KM + n * 256 + d0 * 64 + hi * 32), k1 = *(lds_cf32x4*)(shm3 + LDS_KM + n * 256 + d0 * 64 + hi * 32 + 16);
;                 gate[n] += (float)qv[0] * k0[0] + (float)qv[1] * k0[1] + (float)qv[2] * k0[2] + (float)qv[3] * k0[3] + (float)qv[4] * k1[0] + (float)qv[5] * k1[1] + (float)qv[6] * k1[2] + (float)qv[7] * k1[3];
;             }
;         }
.LBB0_474:
	v_and_b32_e32 v0, 32, v98
	v_add_u32_e32 v0, 0, v0
	v_add_u32_e32 v17, 0x16900, v0
	ds_read_b128 v[18:21], v17
	ds_read_b128 v[22:25], v17 offset:16
	ds_read_b128 v[26:29], v17 offset:256
	ds_read_b128 v[34:37], v17 offset:272
	ds_read_b128 v[38:41], v17 offset:512
	ds_read_b128 v[42:45], v17 offset:528
	ds_read_b128 v[46:49], v17 offset:768
	ds_read_b128 v[50:53], v17 offset:784
	ds_read_b128 v[54:57], v17 offset:1024
	ds_read_b128 v[58:61], v17 offset:1040
	ds_read_b128 v[8:11], v17 offset:1280
	ds_read_b128 v[0:3], v17 offset:1296
	ds_read_b128 v[62:65], v17 offset:1536
	ds_read_b128 v[66:69], v17 offset:1552
	ds_read_b128 v[70:73], v17 offset:64
	ds_read_b128 v[74:77], v17 offset:80
	ds_read_b128 v[78:81], v17 offset:320
	ds_read_b128 v[82:85], v17 offset:336
	ds_read_b128 v[86:89], v17 offset:576
	ds_read_b128 v[90:93], v17 offset:592
	ds_read_b128 v[136:139], v17 offset:832
	ds_read_b128 v[140:143], v17 offset:848
	ds_read_b128 v[144:147], v17 offset:1088
	ds_read_b128 v[148:151], v17 offset:1104
	ds_read_b128 v[12:15], v17 offset:1344
	ds_read_b128 v[4:7], v17 offset:1360
	ds_read_b128 v[152:155], v17 offset:1600
	ds_read_b128 v[156:159], v17 offset:1616
	s_waitcnt vmcnt(0)
	v_cvt_f32_f16_sdwa v95, v124 dst_sel:DWORD dst_unused:UNUSED_PAD src0_sel:WORD_1
	v_cvt_f32_f16_sdwa v94, v128 dst_sel:DWORD dst_unused:UNUSED_PAD src0_sel:WORD_1
	v_cvt_f32_f16_e32 v31, v124
	v_cvt_f32_f16_e32 v30, v128
	v_cvt_f32_f16_e32 v161, v125
	v_cvt_f32_f16_e32 v160, v129
	v_cvt_f32_f16_sdwa v163, v125 dst_sel:DWORD dst_unused:UNUSED_PAD src0_sel:WORD_1
	v_cvt_f32_f16_sdwa v162, v129 dst_sel:DWORD dst_unused:UNUSED_PAD src0_sel:WORD_1
	s_waitcnt lgkmcnt(1)
	v_mov_b32_e32 v173, v152
	v_mov_b32_e32 v152, v63
	v_cvt_f32_f16_e32 v165, v126
	v_cvt_f32_f16_e32 v164, v130
	v_mov_b32_e32 v172, v62
	v_pk_mul_f32 v[62:63], v[152:153], v[94:95]
	v_cvt_f32_f16_sdwa v167, v126 dst_sel:DWORD dst_unused:UNUSED_PAD src0_sel:WORD_1
	v_cvt_f32_f16_sdwa v166, v130 dst_sel:DWORD dst_unused:UNUSED_PAD src0_sel:WORD_1
	v_pk_fma_f32 v[62:63], v[172:173], v[30:31], v[62:63]
	v_mov_b32_e32 v152, v64
	v_mov_b32_e32 v153, v154
	v_cvt_f32_f16_e32 v169, v127
	v_cvt_f32_f16_e32 v168, v131
	v_pk_fma_f32 v[62:63], v[152:153], v[160:161], v[62:63]
	v_mov_b32_e32 v154, v65
	v_pk_fma_f32 v[62:63], v[154:155], v[162:163], v[62:63]
	v_mov_b32_e32 v64, v66
	s_waitcnt lgkmcnt(0)
	v_mov_b32_e32 v65, v156
	v_pk_fma_f32 v[62:63], v[64:65], v[164:165], v[62:63]
	v_mov_b32_e32 v156, v67
	v_pk_fma_f32 v[62:63], v[156:157], v[166:167], v[62:63]
	v_mov_b32_e32 v64, v68
	v_mov_b32_e32 v65, v158
	v_pk_fma_f32 v[62:63], v[64:65], v[168:169], v[62:63]
	v_mov_b32_e32 v65, v70
	v_mov_b32_e32 v70, v19
	v_mov_b32_e32 v64, v18
	v_pk_mul_f32 v[18:19], v[70:71], v[94:95]
	v_cvt_f32_f16_sdwa v171, v127 dst_sel:DWORD dst_unused:UNUSED_PAD src0_sel:WORD_1
	v_pk_fma_f32 v[18:19], v[64:65], v[30:31], v[18:19]
	v_mov_b32_e32 v64, v20
	v_mov_b32_e32 v65, v72
	v_pk_fma_f32 v[18:19], v[64:65], v[160:161], v[18:19]
	v_mov_b32_e32 v72, v21
	v_cvt_f32_f16_sdwa v170, v131 dst_sel:DWORD dst_unused:UNUSED_PAD src0_sel:WORD_1
	v_pk_fma_f32 v[18:19], v[72:73], v[162:163], v[18:19]
	v_mov_b32_e32 v20, v22
	v_mov_b32_e32 v21, v74
	v_pk_fma_f32 v[18:19], v[20:21], v[164:165], v[18:19]
	v_mov_b32_e32 v74, v23
	v_pk_fma_f32 v[18:19], v[74:75], v[166:167], v[18:19]
	v_mov_b32_e32 v20, v24
	v_mov_b32_e32 v21, v76
	v_pk_fma_f32 v[18:19], v[20:21], v[168:169], v[18:19]
	v_mov_b32_e32 v76, v25
	v_pk_fma_f32 v[18:19], v[76:77], v[170:171], v[18:19]
	v_mov_b32_e32 v158, v69
	v_add_f32_e32 v174, v18, v19
	v_mov_b32_e32 v19, v78
	v_mov_b32_e32 v78, v27
	v_mov_b32_e32 v18, v26
	v_pk_mul_f32 v[20:21], v[78:79], v[94:95]
	v_pk_fma_f32 v[62:63], v[158:159], v[170:171], v[62:63]
	v_pk_fma_f32 v[18:19], v[18:19], v[30:31], v[20:21]
	v_mov_b32_e32 v20, v28
	v_mov_b32_e32 v21, v80
	v_pk_fma_f32 v[18:19], v[20:21], v[160:161], v[18:19]
	v_mov_b32_e32 v80, v29
	v_pk_fma_f32 v[18:19], v[80:81], v[162:163], v[18:19]
	v_mov_b32_e32 v20, v34
	v_mov_b32_e32 v21, v82
	v_pk_fma_f32 v[18:19], v[20:21], v[164:165], v[18:19]
	v_mov_b32_e32 v82, v35
	v_pk_fma_f32 v[18:19], v[82:83], v[166:167], v[18:19]
	v_mov_b32_e32 v20, v36
	v_mov_b32_e32 v21, v84
	v_pk_fma_f32 v[18:19], v[20:21], v[168:169], v[18:19]
	v_mov_b32_e32 v84, v37
	v_pk_fma_f32 v[18:19], v[84:85], v[170:171], v[18:19]
	v_add_f32_e32 v33, 0, v62
	v_add_f32_e32 v175, v18, v19
	v_mov_b32_e32 v19, v86
	v_mov_b32_e32 v86, v39
	v_mov_b32_e32 v18, v38
	v_pk_mul_f32 v[20:21], v[86:87], v[94:95]
	v_add_f32_e32 v33, v33, v63
	v_pk_fma_f32 v[18:19], v[18:19], v[30:31], v[20:21]
	v_mov_b32_e32 v20, v40
	v_mov_b32_e32 v21, v88
	v_pk_fma_f32 v[18:19], v[20:21], v[160:161], v[18:19]
	v_mov_b32_e32 v88, v41
	v_pk_fma_f32 v[18:19], v[88:89], v[162:163], v[18:19]
	v_mov_b32_e32 v20, v42
	v_mov_b32_e32 v21, v90
	v_pk_fma_f32 v[18:19], v[20:21], v[164:165], v[18:19]
	v_mov_b32_e32 v90, v43
	v_pk_fma_f32 v[18:19], v[90:91], v[166:167], v[18:19]
	v_mov_b32_e32 v20, v44
	v_mov_b32_e32 v21, v92
	v_pk_fma_f32 v[18:19], v[20:21], v[168:169], v[18:19]
	v_mov_b32_e32 v92, v45
	v_pk_fma_f32 v[18:19], v[92:93], v[170:171], v[18:19]
	s_cmp_lg_u32 s11, 4
	v_add_f32_e32 v176, v18, v19
	v_mov_b32_e32 v19, v136
	v_mov_b32_e32 v136, v47
	v_mov_b32_e32 v18, v46
	v_pk_mul_f32 v[20:21], v[136:137], v[94:95]
	s_cselect_b64 vcc, -1, 0
	v_pk_fma_f32 v[18:19], v[18:19], v[30:31], v[20:21]
	v_mov_b32_e32 v20, v48
	v_mov_b32_e32 v21, v138
	v_pk_fma_f32 v[18:19], v[20:21], v[160:161], v[18:19]
	v_mov_b32_e32 v138, v49
	v_pk_fma_f32 v[18:19], v[138:139], v[162:163], v[18:19]
	v_mov_b32_e32 v20, v50
	v_mov_b32_e32 v21, v140
; template <bool MOBA, int THRL> ...
;     ...
;         for (int d0 = 0; d0 < 4; ++d0) {
;             const h16x8 qv = __builtin_bit_cast(h16x8, qr[d0]);
; #pragma unroll
;             for (int n = 0; n < 7; ++n) {
;                 const f32x4 k0 = *(lds_cf32x4*)(shm3 + LDS_KM + n * 256 + d0 * 64 + hi * 32), k1 = *(lds_cf32x4*)(shm3 + LDS_KM + n * 256 + d0 * 64 + hi * 32 + 16);
;                 gate[n] += (float)qv[0] * k0[0] + (float)qv[1] * k0[1] + (float)qv[2] * k0[2] + (float)qv[3] * k0[3] + (float)qv[4] * k1[0] + (float)qv[5] * k1[1] + (float)qv[6] * k1[2] + (float)qv[7] * k1[3];
;             }
;         }
	v_pk_fma_f32 v[18:19], v[20:21], v[164:165], v[18:19]
	v_mov_b32_e32 v140, v51
	v_pk_fma_f32 v[18:19], v[140:141], v[166:167], v[18:19]
	v_mov_b32_e32 v20, v52
	v_mov_b32_e32 v21, v142
	v_pk_fma_f32 v[18:19], v[20:21], v[168:169], v[18:19]
	v_mov_b32_e32 v142, v53
	v_pk_fma_f32 v[18:19], v[142:143], v[170:171], v[18:19]
	s_cmp_gt_u32 s11, 5
	v_add_f32_e32 v177, v18, v19
	v_mov_b32_e32 v19, v144
	v_mov_b32_e32 v144, v55
	v_mov_b32_e32 v18, v54
	v_pk_mul_f32 v[20:21], v[144:145], v[94:95]
	s_mov_b32 s0, 0xff800000
	v_pk_fma_f32 v[18:19], v[18:19], v[30:31], v[20:21]
	v_mov_b32_e32 v20, v56
	v_mov_b32_e32 v21, v146
	v_pk_fma_f32 v[18:19], v[20:21], v[160:161], v[18:19]
	v_mov_b32_e32 v146, v57
	v_pk_fma_f32 v[18:19], v[146:147], v[162:163], v[18:19]
	v_mov_b32_e32 v20, v58
	v_mov_b32_e32 v21, v148
	v_pk_fma_f32 v[18:19], v[20:21], v[164:165], v[18:19]
	v_mov_b32_e32 v148, v59
	v_pk_fma_f32 v[18:19], v[148:149], v[166:167], v[18:19]
	v_mov_b32_e32 v20, v60
	v_mov_b32_e32 v21, v150
	v_pk_fma_f32 v[18:19], v[20:21], v[168:169], v[18:19]
	v_mov_b32_e32 v150, v61
	v_pk_fma_f32 v[18:19], v[150:151], v[170:171], v[18:19]
	s_nop 0
	v_add_f32_e32 v178, v18, v19
	v_mov_b32_e32 v19, v12
	v_mov_b32_e32 v12, v9
	v_mov_b32_e32 v18, v8
	v_pk_mul_f32 v[8:9], v[12:13], v[94:95]
	v_mov_b32_e32 v12, v10
	v_pk_fma_f32 v[8:9], v[18:19], v[30:31], v[8:9]
	v_mov_b32_e32 v13, v14
	v_pk_fma_f32 v[8:9], v[12:13], v[160:161], v[8:9]
	v_mov_b32_e32 v14, v11
	v_pk_fma_f32 v[8:9], v[14:15], v[162:163], v[8:9]
	v_mov_b32_e32 v10, v0
	v_mov_b32_e32 v11, v4
	v_pk_fma_f32 v[8:9], v[10:11], v[164:165], v[8:9]
	v_mov_b32_e32 v4, v1
	v_pk_fma_f32 v[0:1], v[4:5], v[166:167], v[8:9]
	v_mov_b32_e32 v4, v2
	v_mov_b32_e32 v5, v6
	v_pk_fma_f32 v[0:1], v[4:5], v[168:169], v[0:1]
	v_mov_b32_e32 v6, v3
	v_pk_fma_f32 v[0:1], v[6:7], v[170:171], v[0:1]
	v_cvt_f32_f16_sdwa v95, v116 dst_sel:DWORD dst_unused:UNUSED_PAD src0_sel:WORD_1
	v_add_f32_e32 v179, v0, v1
	ds_read_b128 v[18:21], v17 offset:128
	ds_read_b128 v[22:25], v17 offset:144
	ds_read_b128 v[26:29], v17 offset:384
	ds_read_b128 v[34:37], v17 offset:400
	ds_read_b128 v[38:41], v17 offset:640
	ds_read_b128 v[42:45], v17 offset:656
	ds_read_b128 v[46:49], v17 offset:896
	ds_read_b128 v[50:53], v17 offset:912
	ds_read_b128 v[54:57], v17 offset:1152
	ds_read_b128 v[58:61], v17 offset:1168
	ds_read_b128 v[8:11], v17 offset:1408
	ds_read_b128 v[0:3], v17 offset:1424
	ds_read_b128 v[62:65], v17 offset:1664
	ds_read_b128 v[66:69], v17 offset:1680
	ds_read_b128 v[70:73], v17 offset:192
	ds_read_b128 v[74:77], v17 offset:208
	ds_read_b128 v[78:81], v17 offset:448
	ds_read_b128 v[82:85], v17 offset:464
	ds_read_b128 v[86:89], v17 offset:704
	ds_read_b128 v[90:93], v17 offset:720
	ds_read_b128 v[136:139], v17 offset:960
	ds_read_b128 v[140:143], v17 offset:976
	ds_read_b128 v[144:147], v17 offset:1216
	ds_read_b128 v[148:151], v17 offset:1232
	ds_read_b128 v[12:15], v17 offset:1472
	ds_read_b128 v[4:7], v17 offset:1488
	ds_read_b128 v[152:155], v17 offset:1728
	ds_read_b128 v[156:159], v17 offset:1744
	v_cvt_f32_f16_sdwa v94, v120 dst_sel:DWORD dst_unused:UNUSED_PAD src0_sel:WORD_1
	v_cvt_f32_f16_e32 v31, v116
	v_cvt_f32_f16_e32 v30, v120
	v_cvt_f32_f16_e32 v161, v117
	v_cvt_f32_f16_e32 v160, v121
	v_cvt_f32_f16_sdwa v163, v117 dst_sel:DWORD dst_unused:UNUSED_PAD src0_sel:WORD_1
	v_cvt_f32_f16_sdwa v162, v121 dst_sel:DWORD dst_unused:UNUSED_PAD src0_sel:WORD_1
	s_waitcnt lgkmcnt(1)
	v_mov_b32_e32 v173, v152
	v_mov_b32_e32 v152, v63
	v_cvt_f32_f16_e32 v165, v118
	v_cvt_f32_f16_e32 v164, v122
	v_mov_b32_e32 v172, v62
	v_pk_mul_f32 v[62:63], v[152:153], v[94:95]
	v_cvt_f32_f16_sdwa v167, v118 dst_sel:DWORD dst_unused:UNUSED_PAD src0_sel:WORD_1
	v_cvt_f32_f16_sdwa v166, v122 dst_sel:DWORD dst_unused:UNUSED_PAD src0_sel:WORD_1
	v_pk_fma_f32 v[62:63], v[172:173], v[30:31], v[62:63]
	v_mov_b32_e32 v152, v64
	v_mov_b32_e32 v153, v154
	v_cvt_f32_f16_e32 v169, v119
	v_cvt_f32_f16_e32 v168, v123
	v_pk_fma_f32 v[62:63], v[152:153], v[160:161], v[62:63]
	v_mov_b32_e32 v154, v65
	v_pk_fma_f32 v[62:63], v[154:155], v[162:163], v[62:63]
	v_mov_b32_e32 v64, v66
	s_waitcnt lgkmcnt(0)
	v_mov_b32_e32 v65, v156
	v_pk_fma_f32 v[62:63], v[64:65], v[164:165], v[62:63]
	v_mov_b32_e32 v156, v67
	v_pk_fma_f32 v[62:63], v[156:157], v[166:167], v[62:63]
	v_mov_b32_e32 v64, v68
	v_mov_b32_e32 v65, v158
	v_pk_fma_f32 v[62:63], v[64:65], v[168:169], v[62:63]
	v_mov_b32_e32 v65, v70
	v_mov_b32_e32 v70, v19
	v_mov_b32_e32 v64, v18
	v_pk_mul_f32 v[18:19], v[70:71], v[94:95]
	v_cvt_f32_f16_sdwa v171, v119 dst_sel:DWORD dst_unused:UNUSED_PAD src0_sel:WORD_1
	v_pk_fma_f32 v[18:19], v[64:65], v[30:31], v[18:19]
	v_mov_b32_e32 v64, v20
	v_mov_b32_e32 v65, v72
	v_pk_fma_f32 v[18:19], v[64:65], v[160:161], v[18:19]
	v_mov_b32_e32 v72, v21
	v_cvt_f32_f16_sdwa v170, v123 dst_sel:DWORD dst_unused:UNUSED_PAD src0_sel:WORD_1
	v_pk_fma_f32 v[18:19], v[72:73], v[162:163], v[18:19]
	v_mov_b32_e32 v20, v22
	v_mov_b32_e32 v21, v74
	v_pk_fma_f32 v[18:19], v[20:21], v[164:165], v[18:19]
	v_mov_b32_e32 v74, v23
	v_pk_fma_f32 v[18:19], v[74:75], v[166:167], v[18:19]
	v_mov_b32_e32 v20, v24
	v_mov_b32_e32 v21, v76
	v_pk_fma_f32 v[18:19], v[20:21], v[168:169], v[18:19]
	v_mov_b32_e32 v76, v25
	v_pk_fma_f32 v[18:19], v[76:77], v[170:171], v[18:19]
	v_mov_b32_e32 v158, v69
	v_add_f32_e32 v18, v174, v18
	v_add_f32_e32 v22, v18, v19
	v_mov_b32_e32 v19, v78
	v_mov_b32_e32 v78, v27
	v_mov_b32_e32 v18, v26
	v_pk_mul_f32 v[20:21], v[78:79], v[94:95]
	v_pk_fma_f32 v[62:63], v[158:159], v[170:171], v[62:63]
	v_pk_fma_f32 v[18:19], v[18:19], v[30:31], v[20:21]
	v_mov_b32_e32 v20, v28
	v_mov_b32_e32 v21, v80
; __device__ __forceinline__ float half_sum(float v) { auto rr = __builtin_amdgcn_permlane32_swap(__float_as_uint(v), __float_as_uint(v), false, false); return __uint_as_float(rr[0]) + __uint_as_float(rr[1]); }
; template <bool MOBA, int THRL> ...
;     ...
;         for (int d0 = 0; d0 < 4; ++d0) {
;             const h16x8 qv = __builtin_bit_cast(h16x8, qr[d0]);
; #pragma unroll
;             for (int n = 0; n < 7; ++n) {
;                 const f32x4 k0 = *(lds_cf32x4*)(shm3 + LDS_KM + n * 256 + d0 * 64 + hi * 32), k1 = *(lds_cf32x4*)(shm3 + LDS_KM + n * 256 + d0 * 64 + hi * 32 + 16);
;                 gate[n] += (float)qv[0] * k0[0] + (float)qv[1] * k0[1] + (float)qv[2] * k0[2] + (float)qv[3] * k0[3] + (float)qv[4] * k1[0] + (float)qv[5] * k1[1] + (float)qv[6] * k1[2] + (float)qv[7] * k1[3];
;             }
;         }
; #pragma unroll
;         for (int n = 0; n < 7; ++n) { gate[n] = half_sum(gate[n]); if (n >= qb) gate[n] = -INFINITY; }
	v_pk_fma_f32 v[18:19], v[20:21], v[160:161], v[18:19]
	v_mov_b32_e32 v80, v29
	v_pk_fma_f32 v[18:19], v[80:81], v[162:163], v[18:19]
	v_mov_b32_e32 v20, v34
	v_mov_b32_e32 v21, v82
	v_pk_fma_f32 v[18:19], v[20:21], v[164:165], v[18:19]
	v_mov_b32_e32 v82, v35
	v_pk_fma_f32 v[18:19], v[82:83], v[166:167], v[18:19]
	v_mov_b32_e32 v20, v36
	v_mov_b32_e32 v21, v84
	v_pk_fma_f32 v[18:19], v[20:21], v[168:169], v[18:19]
	v_mov_b32_e32 v84, v37
	v_pk_fma_f32 v[18:19], v[84:85], v[170:171], v[18:19]
	v_add_f32_e32 v17, v33, v62
	v_add_f32_e32 v18, v175, v18
	v_add_f32_e32 v23, v18, v19
	v_mov_b32_e32 v19, v86
	v_mov_b32_e32 v86, v39
	v_mov_b32_e32 v18, v38
	v_pk_mul_f32 v[20:21], v[86:87], v[94:95]
	s_nop 0
	v_pk_fma_f32 v[18:19], v[18:19], v[30:31], v[20:21]
	v_mov_b32_e32 v20, v40
	v_mov_b32_e32 v21, v88
	v_pk_fma_f32 v[18:19], v[20:21], v[160:161], v[18:19]
	v_mov_b32_e32 v88, v41
	v_pk_fma_f32 v[18:19], v[88:89], v[162:163], v[18:19]
	v_mov_b32_e32 v20, v42
	v_mov_b32_e32 v21, v90
	v_pk_fma_f32 v[18:19], v[20:21], v[164:165], v[18:19]
	v_mov_b32_e32 v90, v43
	v_pk_fma_f32 v[18:19], v[90:91], v[166:167], v[18:19]
	v_mov_b32_e32 v20, v44
	v_mov_b32_e32 v21, v92
	v_pk_fma_f32 v[18:19], v[20:21], v[168:169], v[18:19]
	v_mov_b32_e32 v92, v45
	v_pk_fma_f32 v[18:19], v[92:93], v[170:171], v[18:19]
	s_nop 0
	v_add_f32_e32 v18, v176, v18
	v_add_f32_e32 v24, v18, v19
	v_mov_b32_e32 v19, v136
	v_mov_b32_e32 v136, v47
	v_mov_b32_e32 v18, v46
	v_pk_mul_f32 v[20:21], v[136:137], v[94:95]
	s_nop 0
	v_pk_fma_f32 v[18:19], v[18:19], v[30:31], v[20:21]
	v_mov_b32_e32 v20, v48
	v_mov_b32_e32 v21, v138
	v_pk_fma_f32 v[18:19], v[20:21], v[160:161], v[18:19]
	v_mov_b32_e32 v138, v49
	v_pk_fma_f32 v[18:19], v[138:139], v[162:163], v[18:19]
	v_mov_b32_e32 v20, v50
	v_mov_b32_e32 v21, v140
	v_pk_fma_f32 v[18:19], v[20:21], v[164:165], v[18:19]
	v_mov_b32_e32 v140, v51
	v_pk_fma_f32 v[18:19], v[140:141], v[166:167], v[18:19]
	v_mov_b32_e32 v20, v52
	v_mov_b32_e32 v21, v142
	v_pk_fma_f32 v[18:19], v[20:21], v[168:169], v[18:19]
	v_mov_b32_e32 v142, v53
	v_pk_fma_f32 v[18:19], v[142:143], v[170:171], v[18:19]
	s_nop 0
	v_add_f32_e32 v18, v177, v18
	v_add_f32_e32 v25, v18, v19
	v_mov_b32_e32 v19, v144
	v_mov_b32_e32 v144, v55
	v_mov_b32_e32 v18, v54
	v_pk_mul_f32 v[20:21], v[144:145], v[94:95]
	s_nop 0
	v_pk_fma_f32 v[18:19], v[18:19], v[30:31], v[20:21]
	v_mov_b32_e32 v20, v56
	v_mov_b32_e32 v21, v146
	v_pk_fma_f32 v[18:19], v[20:21], v[160:161], v[18:19]
	v_mov_b32_e32 v146, v57
	v_pk_fma_f32 v[18:19], v[146:147], v[162:163], v[18:19]
	v_mov_b32_e32 v20, v58
	v_mov_b32_e32 v21, v148
	v_pk_fma_f32 v[18:19], v[20:21], v[164:165], v[18:19]
	v_mov_b32_e32 v148, v59
	v_pk_fma_f32 v[18:19], v[148:149], v[166:167], v[18:19]
	v_mov_b32_e32 v20, v60
	v_mov_b32_e32 v21, v150
	v_pk_fma_f32 v[18:19], v[20:21], v[168:169], v[18:19]
	v_mov_b32_e32 v150, v61
	v_pk_fma_f32 v[18:19], v[150:151], v[170:171], v[18:19]
	s_nop 0
	v_add_f32_e32 v18, v178, v18
	v_add_f32_e32 v20, v18, v19
	v_mov_b32_e32 v19, v12
	v_mov_b32_e32 v12, v9
	v_mov_b32_e32 v18, v8
	v_pk_mul_f32 v[8:9], v[12:13], v[94:95]
	v_mov_b32_e32 v12, v10
	v_pk_fma_f32 v[8:9], v[18:19], v[30:31], v[8:9]
	v_mov_b32_e32 v13, v14
	v_pk_fma_f32 v[8:9], v[12:13], v[160:161], v[8:9]
	v_mov_b32_e32 v14, v11
	v_pk_fma_f32 v[8:9], v[14:15], v[162:163], v[8:9]
	v_mov_b32_e32 v10, v0
	v_mov_b32_e32 v11, v4
	v_pk_fma_f32 v[8:9], v[10:11], v[164:165], v[8:9]
	v_mov_b32_e32 v4, v1
	v_pk_fma_f32 v[0:1], v[4:5], v[166:167], v[8:9]
	v_mov_b32_e32 v4, v2
	v_mov_b32_e32 v5, v6
	v_pk_fma_f32 v[0:1], v[4:5], v[168:169], v[0:1]
	v_mov_b32_e32 v6, v3
	v_pk_fma_f32 v[0:1], v[6:7], v[170:171], v[0:1]
	v_mov_b32_e32 v6, v20
	v_add_f32_e32 v0, v179, v0
	v_add_f32_e32 v0, v0, v1
	v_mov_b32_e32 v7, v0
	v_add_f32_e32 v1, v17, v63
	v_permlane32_swap_b32_e32 v20, v6
	v_permlane32_swap_b32_e32 v0, v7
	v_mov_b32_e32 v2, v22
	v_add_f32_e32 v6, v20, v6
	v_add_f32_e32 v0, v0, v7
	v_mov_b32_e32 v7, v1
	v_permlane32_swap_b32_e32 v22, v2
	v_cndmask_b32_e32 v6, v248, v6, vcc
; __device__ __forceinline__ float half_sum(float v) { auto rr = __builtin_amdgcn_permlane32_swap(__float_as_uint(v), __float_as_uint(v), false, false); return __uint_as_float(rr[0]) + __uint_as_float(rr[1]); }
; template <bool MOBA, int THRL> ...
;     ...
;         for (int n = 0; n < 7; ++n) { gate[n] = half_sum(gate[n]); if (n >= qb) gate[n] = -INFINITY; }
;         unsigned sb = 0u;
; #pragma unroll
;         for (int r = 0; r < 3; ++r) {
;             float best = -INFINITY; int bi = 0;
; #pragma unroll
;             for (int n = 0; n < 7; ++n) { const bool fr_ = !((sb >> n) & 1u); if (fr_ && gate[n] > best) { best = gate[n]; bi = n; } }
;             sb |= 1u << bi;
;         }
;         selbits = sb;
	s_cselect_b64 vcc, -1, 0
	v_permlane32_swap_b32_e32 v1, v7
	s_cmp_eq_u32 s11, 7
	v_add_f32_e32 v2, v22, v2
	v_mov_b32_e32 v3, v23
	v_cndmask_b32_e32 v0, v248, v0, vcc
	v_add_f32_e32 v1, v1, v7
	s_cselect_b64 vcc, -1, 0
	v_permlane32_swap_b32_e32 v23, v3
	v_cndmask_b32_e32 v1, v248, v1, vcc
	v_cmp_lg_f32_e32 vcc, s0, v2
	v_add_f32_e32 v3, v23, v3
	v_mov_b32_e32 v4, v24
	v_cndmask_b32_e32 v7, v248, v2, vcc
	s_nop 0
	v_permlane32_swap_b32_e32 v24, v4
	v_cmp_gt_f32_e32 vcc, v3, v7
	v_add_f32_e32 v4, v24, v4
	v_mov_b32_e32 v5, v25
	v_cndmask_b32_e32 v7, v7, v3, vcc
	s_nop 0
	v_permlane32_swap_b32_e32 v25, v5
	v_cndmask_b32_e64 v8, 0, 1, vcc
	v_cmp_gt_f32_e32 vcc, v4, v7
	v_add_f32_e32 v5, v25, v5
	v_cmp_nlg_f32_e64 s[0:1], s0, v2
	v_cndmask_b32_e32 v7, v7, v4, vcc
	v_cndmask_b32_e64 v8, v8, 2, vcc
	v_cmp_gt_f32_e32 vcc, v5, v7
	s_nop 1
	v_cndmask_b32_e32 v7, v7, v5, vcc
	v_cndmask_b32_e64 v8, v8, 3, vcc
	v_cmp_gt_f32_e32 vcc, v6, v7
	s_nop 1
	v_cndmask_b32_e32 v7, v7, v6, vcc
	v_cndmask_b32_e64 v8, v8, 4, vcc
	v_cmp_gt_f32_e32 vcc, v0, v7
	s_nop 1
	v_cndmask_b32_e32 v7, v7, v0, vcc
	v_cndmask_b32_e64 v8, v8, 5, vcc
	v_cmp_ngt_f32_e32 vcc, v1, v7
	s_nop 1
	v_cndmask_b32_e32 v7, 6, v8, vcc
	v_cmp_eq_u32_e32 vcc, 0, v7
	v_lshlrev_b32_e64 v8, v7, 1
	s_or_b64 vcc, vcc, s[0:1]
	v_cndmask_b32_e32 v7, v2, v248, vcc
	v_and_b32_e32 v9, 2, v8
	v_cmp_eq_u32_e32 vcc, 0, v9
	v_cmp_gt_f32_e64 s[38:39], v3, v7
	s_and_b64 vcc, vcc, s[38:39]
	v_cndmask_b32_e32 v7, v7, v3, vcc
	v_and_b32_e32 v10, 4, v8
	v_cndmask_b32_e64 v9, 0, 1, vcc
	v_cmp_eq_u32_e32 vcc, 0, v10
	v_cmp_gt_f32_e64 s[38:39], v4, v7
	s_and_b64 vcc, vcc, s[38:39]
	v_cndmask_b32_e32 v7, v7, v4, vcc
	v_and_b32_e32 v10, 8, v8
	v_cmp_eq_u32_e64 s[38:39], 0, v10
	v_cmp_gt_f32_e64 s[40:41], v5, v7
	s_and_b64 s[38:39], s[38:39], s[40:41]
	v_cndmask_b32_e64 v7, v7, v5, s[38:39]
	v_and_b32_e32 v10, 16, v8
	v_cmp_eq_u32_e64 s[40:41], 0, v10
	v_cmp_gt_f32_e64 s[42:43], v6, v7
	s_and_b64 s[40:41], s[40:41], s[42:43]
	v_cndmask_b32_e64 v7, v7, v6, s[40:41]
	v_and_b32_e32 v10, 32, v8
	v_cmp_eq_u32_e64 s[42:43], 0, v10
	v_cmp_gt_f32_e64 s[46:47], v0, v7
	s_and_b64 s[42:43], s[42:43], s[46:47]
	v_cndmask_b32_e64 v7, v7, v0, s[42:43]
	v_cmp_gt_f32_e64 s[50:51], v1, v7
	v_lshlrev_b32_e64 v7, v9, 1
	v_cndmask_b32_e64 v7, v7, 4, vcc
	v_and_b32_e32 v10, 64, v8
	v_cndmask_b32_e64 v7, v7, 8, s[38:39]
	v_cmp_eq_u32_e64 s[46:47], 0, v10
	v_cndmask_b32_e64 v7, v7, 16, s[40:41]
	v_cndmask_b32_e64 v7, v7, 32, s[42:43]
	s_and_b64 s[38:39], s[46:47], s[50:51]
	v_cndmask_b32_e64 v7, v7, 64, s[38:39]
	v_or_b32_e32 v9, v7, v8
	v_and_b32_e32 v10, 1, v9
	v_cmp_eq_u32_e32 vcc, 1, v10
	s_or_b64 vcc, vcc, s[0:1]
	v_bitop3_b32 v10, v7, 2, v8 bitop3:0xc8
	v_cndmask_b32_e32 v2, v2, v248, vcc
	v_cmp_eq_u32_e32 vcc, 0, v10
	v_cmp_gt_f32_e64 s[0:1], v3, v2
	s_and_b64 vcc, vcc, s[0:1]
	v_cndmask_b32_e32 v2, v2, v3, vcc
	v_bitop3_b32 v3, v7, 4, v8 bitop3:0xc8
	v_cndmask_b32_e64 v10, 0, 1, vcc
	v_cmp_eq_u32_e32 vcc, 0, v3
	v_cmp_gt_f32_e64 s[0:1], v4, v2
	s_and_b64 vcc, vcc, s[0:1]
	v_cndmask_b32_e32 v2, v2, v4, vcc
	v_bitop3_b32 v3, v7, 8, v8 bitop3:0xc8
	v_cmp_eq_u32_e64 s[0:1], 0, v3
	v_cmp_gt_f32_e64 s[38:39], v5, v2
	s_and_b64 s[0:1], s[0:1], s[38:39]
	v_cndmask_b32_e64 v2, v2, v5, s[0:1]
	v_bitop3_b32 v3, v7, 16, v8 bitop3:0xc8
	v_cmp_eq_u32_e64 s[38:39], 0, v3
	v_cmp_gt_f32_e64 s[40:41], v6, v2
	s_and_b64 s[38:39], s[38:39], s[40:41]
	v_cndmask_b32_e64 v2, v2, v6, s[38:39]
	v_bitop3_b32 v3, v7, 32, v8 bitop3:0xc8
	v_cmp_eq_u32_e64 s[40:41], 0, v3
	v_cmp_gt_f32_e64 s[42:43], v0, v2
	s_and_b64 s[40:41], s[40:41], s[42:43]
	v_cndmask_b32_e64 v0, v2, v0, s[40:41]
	v_cmp_gt_f32_e64 s[46:47], v1, v0
	v_lshlrev_b32_e64 v0, v10, 1
	v_cndmask_b32_e64 v0, v0, 4, vcc
	v_bitop3_b32 v2, v7, 64, v8 bitop3:0xc8
	v_cndmask_b32_e64 v0, v0, 8, s[0:1]
	v_cmp_eq_u32_e64 s[42:43], 0, v2
	v_cndmask_b32_e64 v0, v0, 16, s[38:39]
	v_cndmask_b32_e64 v0, v0, 32, s[40:41]
	s_and_b64 s[0:1], s[42:43], s[46:47]
	v_cndmask_b32_e64 v0, v0, 64, s[0:1]
	v_or_b32_e32 v231, v0, v9

; __device__ __forceinline__ void cmask(f32x16& p0, f32x16& p1, int jb, int qrel, int hi) {
;     const float NEG = -INFINITY; int kb = 64 * jb + 4 * hi;
; #pragma unroll
;     for (int r = 0; r < 16; ++r) { int kv = kb + (r & 3) + 8 * (r >> 2); if (kv > qrel) p0[r] = NEG; if (kv + 32 > qrel) p1[r] = NEG; }
; }
.LBB0_477:
	v_add_u32_e32 v184, s0, v230
	ds_read_b64_tr_b16 v[180:181], v184 offset:24576
	ds_read_b64_tr_b16 v[182:183], v184 offset:25088
	s_waitcnt lgkmcnt(9)
	v_mfma_f32_32x32x16_f16 v[48:63], v[176:179], v[128:131], v[48:63]
	v_add_f32_e32 v132, v80, v81
	v_add_f32_e32 v132, v82, v132
	v_add_f32_e32 v132, v83, v132
	v_add_f32_e32 v132, v84, v132
	v_add_f32_e32 v132, v85, v132
	v_cvt_pk_f16_f32 v144, v80, v81
	v_cvt_pk_f16_f32 v145, v82, v83
	ds_read_b64_tr_b16 v[176:177], v184 offset:28672
	ds_read_b64_tr_b16 v[178:179], v184 offset:29184
	s_waitcnt lgkmcnt(10)
	v_mfma_f32_32x32x16_f16 v[32:47], v[172:175], v[128:131], v[32:47]
	v_add_f32_e32 v80, v86, v132
	v_add_f32_e32 v80, v87, v80
	v_add_f32_e32 v80, v88, v80
	v_add_f32_e32 v80, v89, v80
	v_cvt_pk_f16_f32 v146, v84, v85
	v_cvt_pk_f16_f32 v147, v86, v87
	ds_read_b64_tr_b16 v[172:173], v184 offset:25600
	ds_read_b64_tr_b16 v[174:175], v184 offset:26112
	s_waitcnt lgkmcnt(11)
	v_mfma_f32_32x32x16_f16 v[48:63], v[168:171], v[124:127], v[48:63]
	v_add_f32_e32 v80, v90, v80
	v_add_f32_e32 v80, v91, v80
	v_add_f32_e32 v80, v92, v80
	v_add_f32_e32 v80, v93, v80
	v_cvt_pk_f16_f32 v140, v88, v89
	v_cvt_pk_f16_f32 v141, v90, v91
	ds_read_b64_tr_b16 v[84:85], v184 offset:29696
	ds_read_b64_tr_b16 v[86:87], v184 offset:30208
	s_waitcnt lgkmcnt(12)
	v_mfma_f32_32x32x16_f16 v[32:47], v[164:167], v[124:127], v[32:47]
	v_add_f32_e32 v80, v94, v80
	v_add_f32_e32 v80, v95, v80
	v_add_f32_e32 v80, v64, v80
	v_add_f32_e32 v88, v65, v80
	v_cvt_pk_f16_f32 v142, v92, v93
	v_cvt_pk_f16_f32 v143, v94, v95
	ds_read_b64_tr_b16 v[80:81], v184 offset:26624
	ds_read_b64_tr_b16 v[82:83], v184 offset:27136
	s_waitcnt lgkmcnt(13)
	v_mfma_f32_32x32x16_f16 v[48:63], v[160:163], v[120:123], v[48:63]
	v_add_f32_e32 v88, v66, v88
	v_add_f32_e32 v88, v67, v88
	v_add_f32_e32 v88, v68, v88
	v_add_f32_e32 v88, v69, v88
	v_cvt_pk_f16_f32 v136, v64, v65
	v_cvt_pk_f16_f32 v137, v66, v67
	ds_read_b64_tr_b16 v[160:161], v184 offset:30720
	ds_read_b64_tr_b16 v[162:163], v184 offset:31232
	s_waitcnt lgkmcnt(14)
	v_mfma_f32_32x32x16_f16 v[32:47], v[152:155], v[120:123], v[32:47]
	v_add_f32_e32 v64, v70, v88
	v_add_f32_e32 v64, v71, v64
	v_add_f32_e32 v64, v72, v64
	v_add_f32_e32 v88, v73, v64
	v_cvt_pk_f16_f32 v138, v68, v69
	v_cvt_pk_f16_f32 v139, v70, v71
	ds_read_b64_tr_b16 v[64:65], v184 offset:27648
	ds_read_b64_tr_b16 v[66:67], v184 offset:28160
	s_waitcnt lgkmcnt(14)
	v_mfma_f32_32x32x16_f16 v[48:63], v[156:159], v[116:119], v[48:63]
	v_add_f32_e32 v68, v74, v88
	v_add_f32_e32 v68, v75, v68
	v_add_f32_e32 v68, v76, v68
	v_add_f32_e32 v68, v77, v68
	v_cvt_pk_f16_f32 v132, v72, v73
	v_cvt_pk_f16_f32 v133, v74, v75
	ds_read_b64_tr_b16 v[152:153], v184 offset:31744
	ds_read_b64_tr_b16 v[154:155], v184 offset:32256
	v_mfma_f32_32x32x16_f16 v[32:47], v[148:151], v[116:119], v[32:47]
	v_add_f32_e32 v68, v78, v68
	v_add_f32_e32 v68, v79, v68
	v_cvt_pk_f16_f32 v134, v76, v77
	v_cvt_pk_f16_f32 v135, v78, v79
	s_add_i32 s0, s70, s89
	s_cmp_lt_u32 s69, 3
	s_cselect_b64 s[40:41], -1, 0
	s_mov_b32 s1, m0
	s_mov_b32 m0, s0
	s_nop 0
	global_load_lds_dwordx4 v[194:195], off
	s_mov_b32 m0, s1
	s_and_b64 s[0:1], s[40:41], exec
	s_cselect_b32 s18, s50, -3
	s_add_i32 s18, s18, s69
	v_mad_i64_i32 v[70:71], s[0:1], s18, v249, v[216:217]
	s_add_i32 s0, s68, s36
	s_mov_b32 s1, m0
	s_mov_b32 m0, s0
	s_nop 0
	global_load_lds_dwordx4 v[70:71], off
	s_mov_b32 m0, s1
	s_cmp_gt_u32 s69, 3
	s_cbranch_scc1 .LBB0_479
	s_mov_b64 s[100:101], exec
	v_sub_u32_e32 v70, v215, v197
	v_add_u32_e32 v70, 0x7b, v70
	v_cmpx_gt_i32_e32 59, v70
	s_nop 3
	s_cbranch_execz .Lmaskx_done_9
	v_mov_b32_e32 v47, v248
	v_cmpx_gt_i32_e32 58, v70
	v_mov_b32_e32 v46, v248
	v_cmpx_gt_i32_e32 57, v70
	v_mov_b32_e32 v45, v248
	v_cmpx_gt_i32_e32 56, v70
	v_mov_b32_e32 v44, v248
	v_cmpx_gt_i32_e32 51, v70
	v_mov_b32_e32 v43, v248
	v_cmpx_gt_i32_e32 50, v70
	v_mov_b32_e32 v42, v248
	v_cmpx_gt_i32_e32 49, v70
	v_mov_b32_e32 v41, v248
	v_cmpx_gt_i32_e32 48, v70
	v_mov_b32_e32 v40, v248
	v_cmpx_gt_i32_e32 43, v70
	v_mov_b32_e32 v39, v248
	v_cmpx_gt_i32_e32 42, v70
	v_mov_b32_e32 v38, v248
	v_cmpx_gt_i32_e32 41, v70
	v_mov_b32_e32 v37, v248
	v_cmpx_gt_i32_e32 40, v70
	v_mov_b32_e32 v36, v248
	v_cmpx_gt_i32_e32 35, v70
	v_mov_b32_e32 v35, v248
	v_cmpx_gt_i32_e32 34, v70
	v_mov_b32_e32 v34, v248
	v_cmpx_gt_i32_e32 33, v70
	v_mov_b32_e32 v33, v248
	v_cmpx_gt_i32_e32 32, v70
	v_mov_b32_e32 v32, v248
	v_cmpx_gt_i32_e32 27, v70
	v_mov_b32_e32 v63, v248
	v_cmpx_gt_i32_e32 26, v70
	v_mov_b32_e32 v62, v248
	v_cmpx_gt_i32_e32 25, v70
	v_mov_b32_e32 v61, v248
	v_cmpx_gt_i32_e32 24, v70
	v_mov_b32_e32 v60, v248
	v_cmpx_gt_i32_e32 19, v70
	v_mov_b32_e32 v59, v248
	v_cmpx_gt_i32_e32 18, v70
	v_mov_b32_e32 v58, v248
	v_cmpx_gt_i32_e32 17, v70
	v_mov_b32_e32 v57, v248
	v_cmpx_gt_i32_e32 16, v70
	v_mov_b32_e32 v56, v248
	v_cmpx_gt_i32_e32 11, v70
	v_mov_b32_e32 v55, v248
	v_cmpx_gt_i32_e32 10, v70
	v_mov_b32_e32 v54, v248
	v_cmpx_gt_i32_e32 9, v70
	v_mov_b32_e32 v53, v248
	v_cmpx_gt_i32_e32 8, v70
	v_mov_b32_e32 v52, v248
	v_cmpx_gt_i32_e32 3, v70
	v_mov_b32_e32 v51, v248
	v_cmpx_gt_i32_e32 2, v70
	v_mov_b32_e32 v50, v248
	v_cmpx_gt_i32_e32 1, v70
	v_mov_b32_e32 v49, v248
	v_cmpx_gt_i32_e32 0, v70
	v_mov_b32_e32 v48, v248

; __device__ __forceinline__ void cmask(f32x16& p0, f32x16& p1, int jb, int qrel, int hi) {
;     const float NEG = -INFINITY; int kb = 64 * jb + 4 * hi;
; #pragma unroll
;     for (int r = 0; r < 16; ++r) { int kv = kb + (r & 3) + 8 * (r >> 2); if (kv > qrel) p0[r] = NEG; if (kv + 32 > qrel) p1[r] = NEG; }
; }
.LBB0_482:
	s_add_i32 s0, s68, 0x2000
	s_cmpk_lg_i32 s68, 0x4000
	s_cselect_b32 s45, s0, 0
	v_add_u32_e32 v160, s70, v230
	ds_read_b64_tr_b16 v[156:157], v160 offset:24576
	ds_read_b64_tr_b16 v[158:159], v160 offset:25088
	v_mfma_f32_32x32x16_f16 v[80:95], v[188:191], v[128:131], v[80:95]
	v_add_f32_e32 v132, v48, v49
	v_add_f32_e32 v132, v50, v132
	v_add_f32_e32 v132, v51, v132
	v_add_f32_e32 v132, v52, v132
	v_add_f32_e32 v132, v53, v132
	v_cvt_pk_f16_f32 v144, v48, v49
	v_cvt_pk_f16_f32 v145, v50, v51
	ds_read_b64_tr_b16 v[152:153], v160 offset:28672
	ds_read_b64_tr_b16 v[154:155], v160 offset:29184
	v_mfma_f32_32x32x16_f16 v[64:79], v[148:151], v[128:131], v[64:79]
	v_add_f32_e32 v48, v54, v132
	v_add_f32_e32 v48, v55, v48
	v_add_f32_e32 v48, v56, v48
	v_add_f32_e32 v48, v57, v48
	v_cvt_pk_f16_f32 v146, v52, v53
	v_cvt_pk_f16_f32 v147, v54, v55
	ds_read_b64_tr_b16 v[148:149], v160 offset:25600
	ds_read_b64_tr_b16 v[150:151], v160 offset:26112
	v_mfma_f32_32x32x16_f16 v[80:95], v[184:187], v[124:127], v[80:95]
	v_add_f32_e32 v48, v58, v48
	v_add_f32_e32 v48, v59, v48
	v_add_f32_e32 v48, v60, v48
	v_add_f32_e32 v48, v61, v48
	v_cvt_pk_f16_f32 v140, v56, v57
	v_cvt_pk_f16_f32 v141, v58, v59
	ds_read_b64_tr_b16 v[52:53], v160 offset:29696
	ds_read_b64_tr_b16 v[54:55], v160 offset:30208
	v_mfma_f32_32x32x16_f16 v[64:79], v[172:175], v[124:127], v[64:79]
	v_add_f32_e32 v48, v62, v48
	v_add_f32_e32 v48, v63, v48
	v_add_f32_e32 v48, v32, v48
	v_add_f32_e32 v56, v33, v48
	v_cvt_pk_f16_f32 v142, v60, v61
	v_cvt_pk_f16_f32 v143, v62, v63
	ds_read_b64_tr_b16 v[48:49], v160 offset:26624
	ds_read_b64_tr_b16 v[50:51], v160 offset:27136
	s_waitcnt lgkmcnt(13)
	v_mfma_f32_32x32x16_f16 v[80:95], v[176:179], v[120:123], v[80:95]
	v_add_f32_e32 v56, v34, v56
	v_add_f32_e32 v56, v35, v56
	v_add_f32_e32 v56, v36, v56
	v_add_f32_e32 v56, v37, v56
	v_cvt_pk_f16_f32 v136, v32, v33
	v_cvt_pk_f16_f32 v137, v34, v35
	ds_read_b64_tr_b16 v[184:185], v160 offset:30720
	ds_read_b64_tr_b16 v[186:187], v160 offset:31232
	s_waitcnt lgkmcnt(14)
	v_mfma_f32_32x32x16_f16 v[64:79], v[164:167], v[120:123], v[64:79]
	v_add_f32_e32 v32, v38, v56
	v_add_f32_e32 v32, v39, v32
	v_add_f32_e32 v32, v40, v32
	v_add_f32_e32 v56, v41, v32
	v_cvt_pk_f16_f32 v138, v36, v37
	v_cvt_pk_f16_f32 v139, v38, v39
	ds_read_b64_tr_b16 v[32:33], v160 offset:27648
	ds_read_b64_tr_b16 v[34:35], v160 offset:28160
	s_waitcnt lgkmcnt(14)
	v_mfma_f32_32x32x16_f16 v[80:95], v[180:183], v[116:119], v[80:95]
	v_add_f32_e32 v36, v42, v56
	v_add_f32_e32 v36, v43, v36
	v_add_f32_e32 v36, v44, v36
	v_add_f32_e32 v36, v45, v36
	v_cvt_pk_f16_f32 v132, v40, v41
	v_cvt_pk_f16_f32 v133, v42, v43
	ds_read_b64_tr_b16 v[180:181], v160 offset:31744
	ds_read_b64_tr_b16 v[182:183], v160 offset:32256
	v_mfma_f32_32x32x16_f16 v[64:79], v[168:171], v[116:119], v[64:79]
	v_add_f32_e32 v36, v46, v36
	v_add_f32_e32 v36, v47, v36
	v_cvt_pk_f16_f32 v134, v44, v45
	v_cvt_pk_f16_f32 v135, v46, v47
	s_add_i32 s0, s68, s89
	v_lshl_add_u64 v[38:39], v[194:195], 0, s[30:31]
	s_mov_b32 s1, m0
	s_mov_b32 m0, s0
	s_nop 0
	global_load_lds_dwordx4 v[38:39], off
	s_mov_b32 m0, s1
	s_cmp_lt_u32 s69, 2
	s_cselect_b64 s[0:1], -1, 0
	s_and_b64 s[18:19], s[0:1], exec
	s_cselect_b32 s18, s51, -2
	s_add_i32 s18, s18, s69
	v_mad_i64_i32 v[38:39], s[46:47], s18, v249, v[216:217]
	s_add_i32 s19, s45, s36
	s_mov_b32 s46, m0
	s_mov_b32 m0, s19
	s_nop 0
	global_load_lds_dwordx4 v[38:39], off
	s_mov_b32 m0, s46
	s_andn2_b64 vcc, exec, s[40:41]
	s_cbranch_vccnz .LBB0_484
	s_mov_b64 s[100:101], exec
	v_sub_u32_e32 v38, v215, v197
	v_add_u32_e32 v38, 59, v38
	v_cmpx_gt_i32_e32 59, v38
	s_nop 3
	s_cbranch_execz .Lmaskx_done_8
	v_mov_b32_e32 v79, v248
	v_cmpx_gt_i32_e32 58, v38
	v_mov_b32_e32 v78, v248
	v_cmpx_gt_i32_e32 57, v38
	v_mov_b32_e32 v77, v248
	v_cmpx_gt_i32_e32 56, v38
	v_mov_b32_e32 v76, v248
	v_cmpx_gt_i32_e32 51, v38
	v_mov_b32_e32 v75, v248
	v_cmpx_gt_i32_e32 50, v38
	v_mov_b32_e32 v74, v248
	v_cmpx_gt_i32_e32 49, v38
	v_mov_b32_e32 v73, v248
	v_cmpx_gt_i32_e32 48, v38
	v_mov_b32_e32 v72, v248
	v_cmpx_gt_i32_e32 43, v38
	v_mov_b32_e32 v71, v248
	v_cmpx_gt_i32_e32 42, v38
	v_mov_b32_e32 v70, v248
	v_cmpx_gt_i32_e32 41, v38
	v_mov_b32_e32 v69, v248
	v_cmpx_gt_i32_e32 40, v38
	v_mov_b32_e32 v68, v248
	v_cmpx_gt_i32_e32 35, v38
	v_mov_b32_e32 v67, v248
	v_cmpx_gt_i32_e32 34, v38
	v_mov_b32_e32 v66, v248
	v_cmpx_gt_i32_e32 33, v38
	v_mov_b32_e32 v65, v248
	v_cmpx_gt_i32_e32 32, v38
	v_mov_b32_e32 v64, v248
	v_cmpx_gt_i32_e32 27, v38
	v_mov_b32_e32 v95, v248
	v_cmpx_gt_i32_e32 26, v38
	v_mov_b32_e32 v94, v248
	v_cmpx_gt_i32_e32 25, v38
	v_mov_b32_e32 v93, v248
	v_cmpx_gt_i32_e32 24, v38
	v_mov_b32_e32 v92, v248
	v_cmpx_gt_i32_e32 19, v38
	v_mov_b32_e32 v91, v248
	v_cmpx_gt_i32_e32 18, v38
	v_mov_b32_e32 v90, v248
	v_cmpx_gt_i32_e32 17, v38
	v_mov_b32_e32 v89, v248
	v_cmpx_gt_i32_e32 16, v38
	v_mov_b32_e32 v88, v248
	v_cmpx_gt_i32_e32 11, v38
	v_mov_b32_e32 v87, v248
	v_cmpx_gt_i32_e32 10, v38
	v_mov_b32_e32 v86, v248
	v_cmpx_gt_i32_e32 9, v38
	v_mov_b32_e32 v85, v248
	v_cmpx_gt_i32_e32 8, v38
	v_mov_b32_e32 v84, v248
	v_cmpx_gt_i32_e32 3, v38
	v_mov_b32_e32 v83, v248
	v_cmpx_gt_i32_e32 2, v38
	v_mov_b32_e32 v82, v248
	v_cmpx_gt_i32_e32 1, v38
	v_mov_b32_e32 v81, v248
	v_cmpx_gt_i32_e32 0, v38
	v_mov_b32_e32 v80, v248

; __device__ __forceinline__ void cmask(f32x16& p0, f32x16& p1, int jb, int qrel, int hi) {
;     const float NEG = -INFINITY; int kb = 64 * jb + 4 * hi;
; #pragma unroll
;     for (int r = 0; r < 16; ++r) { int kv = kb + (r & 3) + 8 * (r >> 2); if (kv > qrel) p0[r] = NEG; if (kv + 32 > qrel) p1[r] = NEG; }
; }
.LBB0_565:
	v_add_u32_e32 v184, s18, v230
	ds_read_b64_tr_b16 v[180:181], v184 offset:24576
	ds_read_b64_tr_b16 v[182:183], v184 offset:25088
	s_waitcnt lgkmcnt(9)
	v_mfma_f32_32x32x16_f16 v[48:63], v[176:179], v[128:131], v[48:63]
	v_add_f32_e32 v132, v80, v81
	v_add_f32_e32 v132, v82, v132
	v_add_f32_e32 v132, v83, v132
	v_add_f32_e32 v132, v84, v132
	v_add_f32_e32 v132, v85, v132
	v_cvt_pk_f16_f32 v144, v80, v81
	v_cvt_pk_f16_f32 v145, v82, v83
	ds_read_b64_tr_b16 v[80:81], v184 offset:28672
	ds_read_b64_tr_b16 v[82:83], v184 offset:29184
	s_waitcnt lgkmcnt(10)
	v_mfma_f32_32x32x16_f16 v[32:47], v[172:175], v[128:131], v[32:47]
	v_add_f32_e32 v128, v86, v132
	v_add_f32_e32 v128, v87, v128
	v_add_f32_e32 v128, v88, v128
	v_add_f32_e32 v128, v89, v128
	v_cvt_pk_f16_f32 v146, v84, v85
	v_cvt_pk_f16_f32 v147, v86, v87
	ds_read_b64_tr_b16 v[84:85], v184 offset:25600
	ds_read_b64_tr_b16 v[86:87], v184 offset:26112
	s_waitcnt lgkmcnt(11)
	v_mfma_f32_32x32x16_f16 v[48:63], v[168:171], v[124:127], v[48:63]
	v_add_f32_e32 v128, v90, v128
	v_add_f32_e32 v128, v91, v128
	v_add_f32_e32 v128, v92, v128
	v_add_f32_e32 v128, v93, v128
	v_cvt_pk_f16_f32 v140, v88, v89
	v_cvt_pk_f16_f32 v141, v90, v91
	ds_read_b64_tr_b16 v[88:89], v184 offset:29696
	ds_read_b64_tr_b16 v[90:91], v184 offset:30208
	s_waitcnt lgkmcnt(12)
	v_mfma_f32_32x32x16_f16 v[32:47], v[164:167], v[124:127], v[32:47]
	v_add_f32_e32 v124, v94, v128
	v_add_f32_e32 v124, v95, v124
	v_add_f32_e32 v124, v64, v124
	v_add_f32_e32 v124, v65, v124
	v_cvt_pk_f16_f32 v142, v92, v93
	v_cvt_pk_f16_f32 v143, v94, v95
	ds_read_b64_tr_b16 v[92:93], v184 offset:26624
	ds_read_b64_tr_b16 v[94:95], v184 offset:27136
	s_waitcnt lgkmcnt(13)
	v_mfma_f32_32x32x16_f16 v[48:63], v[160:163], v[120:123], v[48:63]
	v_add_f32_e32 v124, v66, v124
	v_add_f32_e32 v124, v67, v124
	v_add_f32_e32 v124, v68, v124
	v_add_f32_e32 v124, v69, v124
	v_cvt_pk_f16_f32 v136, v64, v65
	v_cvt_pk_f16_f32 v137, v66, v67
	ds_read_b64_tr_b16 v[64:65], v184 offset:30720
	ds_read_b64_tr_b16 v[66:67], v184 offset:31232
	s_waitcnt lgkmcnt(14)
	v_mfma_f32_32x32x16_f16 v[32:47], v[152:155], v[120:123], v[32:47]
	v_add_f32_e32 v120, v70, v124
	v_add_f32_e32 v120, v71, v120
	v_add_f32_e32 v120, v72, v120
	v_add_f32_e32 v120, v73, v120
	v_cvt_pk_f16_f32 v138, v68, v69
	v_cvt_pk_f16_f32 v139, v70, v71
	ds_read_b64_tr_b16 v[68:69], v184 offset:27648
	ds_read_b64_tr_b16 v[70:71], v184 offset:28160
	s_waitcnt lgkmcnt(14)
	v_mfma_f32_32x32x16_f16 v[48:63], v[156:159], v[116:119], v[48:63]
	v_add_f32_e32 v120, v74, v120
	v_add_f32_e32 v120, v75, v120
	v_add_f32_e32 v120, v76, v120
	v_add_f32_e32 v120, v77, v120
	v_cvt_pk_f16_f32 v132, v72, v73
	v_cvt_pk_f16_f32 v133, v74, v75
	ds_read_b64_tr_b16 v[72:73], v184 offset:31744
	ds_read_b64_tr_b16 v[74:75], v184 offset:32256
	v_mfma_f32_32x32x16_f16 v[32:47], v[148:151], v[116:119], v[32:47]
	v_add_f32_e32 v116, v78, v120
	v_add_f32_e32 v116, v79, v116
	v_cvt_pk_f16_f32 v134, v76, v77
	v_cvt_pk_f16_f32 v135, v78, v79
	s_andn2_b64 vcc, exec, s[42:43]
	s_cbranch_vccnz .LBB0_567
	s_mov_b64 s[100:101], exec
	v_sub_u32_e32 v77, v215, v233
	v_add_u32_e32 v77, 0xffffff40, v77
	v_cmpx_gt_i32_e32 59, v77
	s_nop 3
	s_cbranch_execz .Lmaskx_done_5
	v_mov_b32_e32 v47, v248
	v_cmpx_gt_i32_e32 58, v77
	v_mov_b32_e32 v46, v248
	v_cmpx_gt_i32_e32 57, v77
	v_mov_b32_e32 v45, v248
	v_cmpx_gt_i32_e32 56, v77
	v_mov_b32_e32 v44, v248
	v_cmpx_gt_i32_e32 51, v77
	v_mov_b32_e32 v43, v248
	v_cmpx_gt_i32_e32 50, v77
	v_mov_b32_e32 v42, v248
	v_cmpx_gt_i32_e32 49, v77
	v_mov_b32_e32 v41, v248
	v_cmpx_gt_i32_e32 48, v77
	v_mov_b32_e32 v40, v248
	v_cmpx_gt_i32_e32 43, v77
	v_mov_b32_e32 v39, v248
	v_cmpx_gt_i32_e32 42, v77
	v_mov_b32_e32 v38, v248
	v_cmpx_gt_i32_e32 41, v77
	v_mov_b32_e32 v37, v248
	v_cmpx_gt_i32_e32 40, v77
	v_mov_b32_e32 v36, v248
	v_cmpx_gt_i32_e32 35, v77
	v_mov_b32_e32 v35, v248
	v_cmpx_gt_i32_e32 34, v77
	v_mov_b32_e32 v34, v248
	v_cmpx_gt_i32_e32 33, v77
	v_mov_b32_e32 v33, v248
	v_cmpx_gt_i32_e32 32, v77
	v_mov_b32_e32 v32, v248
	v_cmpx_gt_i32_e32 27, v77
	v_mov_b32_e32 v63, v248
	v_cmpx_gt_i32_e32 26, v77
	v_mov_b32_e32 v62, v248
	v_cmpx_gt_i32_e32 25, v77
	v_mov_b32_e32 v61, v248
	v_cmpx_gt_i32_e32 24, v77
	v_mov_b32_e32 v60, v248
	v_cmpx_gt_i32_e32 19, v77
	v_mov_b32_e32 v59, v248
	v_cmpx_gt_i32_e32 18, v77
	v_mov_b32_e32 v58, v248
	v_cmpx_gt_i32_e32 17, v77
	v_mov_b32_e32 v57, v248
	v_cmpx_gt_i32_e32 16, v77
	v_mov_b32_e32 v56, v248
	v_cmpx_gt_i32_e32 11, v77
	v_mov_b32_e32 v55, v248
	v_cmpx_gt_i32_e32 10, v77
	v_mov_b32_e32 v54, v248
	v_cmpx_gt_i32_e32 9, v77
	v_mov_b32_e32 v53, v248
	v_cmpx_gt_i32_e32 8, v77
	v_mov_b32_e32 v52, v248
	v_cmpx_gt_i32_e32 3, v77
	v_mov_b32_e32 v51, v248
	v_cmpx_gt_i32_e32 2, v77
	v_mov_b32_e32 v50, v248
	v_cmpx_gt_i32_e32 1, v77
	v_mov_b32_e32 v49, v248
	v_cmpx_gt_i32_e32 0, v77
	v_mov_b32_e32 v48, v248

; __device__ __forceinline__ void cmask(f32x16& p0, f32x16& p1, int jb, int qrel, int hi) {
;     const float NEG = -INFINITY; int kb = 64 * jb + 4 * hi;
; #pragma unroll
;     for (int r = 0; r < 16; ++r) { int kv = kb + (r & 3) + 8 * (r >> 2); if (kv > qrel) p0[r] = NEG; if (kv + 32 > qrel) p1[r] = NEG; }
; }
.LBB0_625:
	v_add_u32_e32 v184, s40, v229
	ds_read_b64_tr_b16 v[180:181], v184 offset:24576
	ds_read_b64_tr_b16 v[182:183], v184 offset:25088
	s_waitcnt lgkmcnt(9)
	v_mfma_f32_32x32x16_f16 v[48:63], v[176:179], v[128:131], v[48:63]
	v_add_f32_e32 v132, v80, v81
	v_add_f32_e32 v132, v82, v132
	v_add_f32_e32 v132, v83, v132
	v_add_f32_e32 v132, v84, v132
	v_add_f32_e32 v132, v85, v132
	v_cvt_pk_f16_f32 v144, v80, v81
	v_cvt_pk_f16_f32 v145, v82, v83
	ds_read_b64_tr_b16 v[176:177], v184 offset:28672
	ds_read_b64_tr_b16 v[178:179], v184 offset:29184
	s_waitcnt lgkmcnt(10)
	v_mfma_f32_32x32x16_f16 v[32:47], v[172:175], v[128:131], v[32:47]
	v_add_f32_e32 v80, v86, v132
	v_add_f32_e32 v80, v87, v80
	v_add_f32_e32 v80, v88, v80
	v_add_f32_e32 v80, v89, v80
	v_cvt_pk_f16_f32 v146, v84, v85
	v_cvt_pk_f16_f32 v147, v86, v87
	ds_read_b64_tr_b16 v[172:173], v184 offset:25600
	ds_read_b64_tr_b16 v[174:175], v184 offset:26112
	s_waitcnt lgkmcnt(11)
	v_mfma_f32_32x32x16_f16 v[48:63], v[168:171], v[124:127], v[48:63]
	v_add_f32_e32 v80, v90, v80
	v_add_f32_e32 v80, v91, v80
	v_add_f32_e32 v80, v92, v80
	v_add_f32_e32 v80, v93, v80
	v_cvt_pk_f16_f32 v140, v88, v89
	v_cvt_pk_f16_f32 v141, v90, v91
	ds_read_b64_tr_b16 v[84:85], v184 offset:29696
	ds_read_b64_tr_b16 v[86:87], v184 offset:30208
	s_waitcnt lgkmcnt(12)
	v_mfma_f32_32x32x16_f16 v[32:47], v[164:167], v[124:127], v[32:47]
	v_add_f32_e32 v80, v94, v80
	v_add_f32_e32 v80, v95, v80
	v_add_f32_e32 v80, v64, v80
	v_add_f32_e32 v88, v65, v80
	v_cvt_pk_f16_f32 v142, v92, v93
	v_cvt_pk_f16_f32 v143, v94, v95
	ds_read_b64_tr_b16 v[80:81], v184 offset:26624
	ds_read_b64_tr_b16 v[82:83], v184 offset:27136
	s_waitcnt lgkmcnt(13)
	v_mfma_f32_32x32x16_f16 v[48:63], v[160:163], v[120:123], v[48:63]
	v_add_f32_e32 v88, v66, v88
	v_add_f32_e32 v88, v67, v88
	v_add_f32_e32 v88, v68, v88
	v_add_f32_e32 v88, v69, v88
	v_cvt_pk_f16_f32 v136, v64, v65
	v_cvt_pk_f16_f32 v137, v66, v67
	ds_read_b64_tr_b16 v[160:161], v184 offset:30720
	ds_read_b64_tr_b16 v[162:163], v184 offset:31232
	s_waitcnt lgkmcnt(14)
	v_mfma_f32_32x32x16_f16 v[32:47], v[152:155], v[120:123], v[32:47]
	v_add_f32_e32 v64, v70, v88
	v_add_f32_e32 v64, v71, v64
	v_add_f32_e32 v64, v72, v64
	v_add_f32_e32 v88, v73, v64
	v_cvt_pk_f16_f32 v138, v68, v69
	v_cvt_pk_f16_f32 v139, v70, v71
	ds_read_b64_tr_b16 v[64:65], v184 offset:27648
	ds_read_b64_tr_b16 v[66:67], v184 offset:28160
	s_waitcnt lgkmcnt(14)
	v_mfma_f32_32x32x16_f16 v[48:63], v[156:159], v[116:119], v[48:63]
	v_add_f32_e32 v68, v74, v88
	v_add_f32_e32 v68, v75, v68
	v_add_f32_e32 v68, v76, v68
	v_add_f32_e32 v68, v77, v68
	v_cvt_pk_f16_f32 v132, v72, v73
	v_cvt_pk_f16_f32 v133, v74, v75
	ds_read_b64_tr_b16 v[152:153], v184 offset:31744
	ds_read_b64_tr_b16 v[154:155], v184 offset:32256
	v_mfma_f32_32x32x16_f16 v[32:47], v[148:151], v[116:119], v[32:47]
	v_add_f32_e32 v68, v78, v68
	v_add_f32_e32 v68, v79, v68
	v_cvt_pk_f16_f32 v134, v76, v77
	v_cvt_pk_f16_f32 v135, v78, v79
	v_lshl_add_u64 v[70:71], v[194:195], 0, s[30:31]
	s_add_i32 s11, s69, s90
	s_mov_b32 s18, m0
	s_mov_b32 m0, s11
	s_nop 0
	global_load_lds_dwordx4 v[70:71], off
	s_mov_b32 m0, s18
	s_add_i32 s18, s26, s45
	s_add_i32 s37, s26, s19
	s_add_i32 s11, s18, 1
	s_add_i32 s66, s37, 1
	s_cmp_lt_u32 s45, 3
	s_cselect_b64 s[40:41], -1, 0
	s_and_b64 s[50:51], s[40:41], exec
	s_cselect_b32 s11, s11, s66
	v_mad_i64_i32 v[70:71], s[50:51], s11, v249, v[216:217]
	s_add_i32 s50, s68, s10
	s_mov_b32 s51, m0
	s_mov_b32 m0, s50
	s_nop 0
	global_load_lds_dwordx4 v[70:71], off
	s_mov_b32 m0, s51
	s_cmp_gt_u32 s45, 3
	s_cbranch_scc1 .LBB0_627
	s_mov_b64 s[100:101], exec
	v_sub_u32_e32 v69, v215, v196
	v_add_u32_e32 v69, 32, v69
	v_cmpx_gt_i32_e32 59, v69
	s_nop 3
	s_cbranch_execz .Lmaskx_done_4
	v_mov_b32_e32 v47, v248
	v_cmpx_gt_i32_e32 58, v69
	v_mov_b32_e32 v46, v248
	v_cmpx_gt_i32_e32 57, v69
	v_mov_b32_e32 v45, v248
	v_cmpx_gt_i32_e32 56, v69
	v_mov_b32_e32 v44, v248
	v_cmpx_gt_i32_e32 51, v69
	v_mov_b32_e32 v43, v248
	v_cmpx_gt_i32_e32 50, v69
	v_mov_b32_e32 v42, v248
	v_cmpx_gt_i32_e32 49, v69
	v_mov_b32_e32 v41, v248
	v_cmpx_gt_i32_e32 48, v69
	v_mov_b32_e32 v40, v248
	v_cmpx_gt_i32_e32 43, v69
	v_mov_b32_e32 v39, v248
	v_cmpx_gt_i32_e32 42, v69
	v_mov_b32_e32 v38, v248
	v_cmpx_gt_i32_e32 41, v69
	v_mov_b32_e32 v37, v248
	v_cmpx_gt_i32_e32 40, v69
	v_mov_b32_e32 v36, v248
	v_cmpx_gt_i32_e32 35, v69
	v_mov_b32_e32 v35, v248
	v_cmpx_gt_i32_e32 34, v69
	v_mov_b32_e32 v34, v248
	v_cmpx_gt_i32_e32 33, v69
	v_mov_b32_e32 v33, v248
	v_cmpx_gt_i32_e32 32, v69
	v_mov_b32_e32 v32, v248
	v_cmpx_gt_i32_e32 27, v69
	v_mov_b32_e32 v63, v248
	v_cmpx_gt_i32_e32 26, v69
	v_mov_b32_e32 v62, v248
	v_cmpx_gt_i32_e32 25, v69
	v_mov_b32_e32 v61, v248
	v_cmpx_gt_i32_e32 24, v69
	v_mov_b32_e32 v60, v248
	v_cmpx_gt_i32_e32 19, v69
	v_mov_b32_e32 v59, v248
	v_cmpx_gt_i32_e32 18, v69
	v_mov_b32_e32 v58, v248
	v_cmpx_gt_i32_e32 17, v69
	v_mov_b32_e32 v57, v248
	v_cmpx_gt_i32_e32 16, v69
	v_mov_b32_e32 v56, v248
	v_cmpx_gt_i32_e32 11, v69
	v_mov_b32_e32 v55, v248
	v_cmpx_gt_i32_e32 10, v69
	v_mov_b32_e32 v54, v248
	v_cmpx_gt_i32_e32 9, v69
	v_mov_b32_e32 v53, v248
	v_cmpx_gt_i32_e32 8, v69
	v_mov_b32_e32 v52, v248
	v_cmpx_gt_i32_e32 3, v69
	v_mov_b32_e32 v51, v248
	v_cmpx_gt_i32_e32 2, v69
	v_mov_b32_e32 v50, v248
	v_cmpx_gt_i32_e32 1, v69
	v_mov_b32_e32 v49, v248
	v_cmpx_gt_i32_e32 0, v69
	v_mov_b32_e32 v48, v248

; __device__ __forceinline__ void cmask(f32x16& p0, f32x16& p1, int jb, int qrel, int hi) {
;     const float NEG = -INFINITY; int kb = 64 * jb + 4 * hi;
; #pragma unroll
;     for (int r = 0; r < 16; ++r) { int kv = kb + (r & 3) + 8 * (r >> 2); if (kv > qrel) p0[r] = NEG; if (kv + 32 > qrel) p1[r] = NEG; }
; }
.LBB0_630:
	s_add_i32 s11, s68, 0x2000
	s_cmpk_lg_i32 s68, 0x4000
	s_cselect_b32 s11, s11, 0
	v_add_u32_e32 v160, s69, v229
	ds_read_b64_tr_b16 v[156:157], v160 offset:24576
	ds_read_b64_tr_b16 v[158:159], v160 offset:25088
	v_mfma_f32_32x32x16_f16 v[80:95], v[188:191], v[128:131], v[80:95]
	v_add_f32_e32 v132, v48, v49
	v_add_f32_e32 v132, v50, v132
	v_add_f32_e32 v132, v51, v132
	v_add_f32_e32 v132, v52, v132
	v_add_f32_e32 v132, v53, v132
	v_cvt_pk_f16_f32 v144, v48, v49
	v_cvt_pk_f16_f32 v145, v50, v51
	ds_read_b64_tr_b16 v[152:153], v160 offset:28672
	ds_read_b64_tr_b16 v[154:155], v160 offset:29184
	v_mfma_f32_32x32x16_f16 v[64:79], v[148:151], v[128:131], v[64:79]
	v_add_f32_e32 v48, v54, v132
	v_add_f32_e32 v48, v55, v48
	v_add_f32_e32 v48, v56, v48
	v_add_f32_e32 v48, v57, v48
	v_cvt_pk_f16_f32 v146, v52, v53
	v_cvt_pk_f16_f32 v147, v54, v55
	ds_read_b64_tr_b16 v[148:149], v160 offset:25600
	ds_read_b64_tr_b16 v[150:151], v160 offset:26112
	v_mfma_f32_32x32x16_f16 v[80:95], v[184:187], v[124:127], v[80:95]
	v_add_f32_e32 v48, v58, v48
	v_add_f32_e32 v48, v59, v48
	v_add_f32_e32 v48, v60, v48
	v_add_f32_e32 v48, v61, v48
	v_cvt_pk_f16_f32 v140, v56, v57
	v_cvt_pk_f16_f32 v141, v58, v59
	ds_read_b64_tr_b16 v[52:53], v160 offset:29696
	ds_read_b64_tr_b16 v[54:55], v160 offset:30208
	v_mfma_f32_32x32x16_f16 v[64:79], v[172:175], v[124:127], v[64:79]
	v_add_f32_e32 v48, v62, v48
	v_add_f32_e32 v48, v63, v48
	v_add_f32_e32 v48, v32, v48
	v_add_f32_e32 v56, v33, v48
	v_cvt_pk_f16_f32 v142, v60, v61
	v_cvt_pk_f16_f32 v143, v62, v63
	ds_read_b64_tr_b16 v[48:49], v160 offset:26624
	ds_read_b64_tr_b16 v[50:51], v160 offset:27136
	s_waitcnt lgkmcnt(13)
	v_mfma_f32_32x32x16_f16 v[80:95], v[176:179], v[120:123], v[80:95]
	v_add_f32_e32 v56, v34, v56
	v_add_f32_e32 v56, v35, v56
	v_add_f32_e32 v56, v36, v56
	v_add_f32_e32 v56, v37, v56
	v_cvt_pk_f16_f32 v136, v32, v33
	v_cvt_pk_f16_f32 v137, v34, v35
	ds_read_b64_tr_b16 v[184:185], v160 offset:30720
	ds_read_b64_tr_b16 v[186:187], v160 offset:31232
	s_waitcnt lgkmcnt(14)
	v_mfma_f32_32x32x16_f16 v[64:79], v[164:167], v[120:123], v[64:79]
	v_add_f32_e32 v32, v38, v56
	v_add_f32_e32 v32, v39, v32
	v_add_f32_e32 v32, v40, v32
	v_add_f32_e32 v56, v41, v32
	v_cvt_pk_f16_f32 v138, v36, v37
	v_cvt_pk_f16_f32 v139, v38, v39
	ds_read_b64_tr_b16 v[32:33], v160 offset:27648
	ds_read_b64_tr_b16 v[34:35], v160 offset:28160
	s_waitcnt lgkmcnt(14)
	v_mfma_f32_32x32x16_f16 v[80:95], v[180:183], v[116:119], v[80:95]
	v_add_f32_e32 v36, v42, v56
	v_add_f32_e32 v36, v43, v36
	v_add_f32_e32 v36, v44, v36
	v_add_f32_e32 v36, v45, v36
	v_cvt_pk_f16_f32 v132, v40, v41
	v_cvt_pk_f16_f32 v133, v42, v43
	ds_read_b64_tr_b16 v[180:181], v160 offset:31744
	ds_read_b64_tr_b16 v[182:183], v160 offset:32256
	v_mfma_f32_32x32x16_f16 v[64:79], v[168:171], v[116:119], v[64:79]
	v_add_f32_e32 v36, v46, v36
	v_add_f32_e32 v36, v47, v36
	v_cvt_pk_f16_f32 v134, v44, v45
	v_cvt_pk_f16_f32 v135, v46, v47
	s_add_i32 s50, s68, s90
	s_add_i32 s18, s18, 2
	s_cmp_lt_u32 s45, 2
	s_mov_b32 s51, m0
	s_mov_b32 m0, s50
	s_nop 0
	global_load_lds_dwordx4 v[194:195], off
	s_mov_b32 m0, s51
	s_cselect_b32 s18, s18, s37
	v_mad_i64_i32 v[38:39], s[50:51], s18, v249, v[216:217]
	s_add_i32 s37, s11, s10
	s_mov_b32 s50, m0
	s_mov_b32 m0, s37
	s_nop 0
	global_load_lds_dwordx4 v[38:39], off
	s_mov_b32 m0, s50
	s_andn2_b64 vcc, exec, s[40:41]
	s_cbranch_vccnz .LBB0_632
	s_mov_b64 s[100:101], exec
	v_sub_u32_e32 v38, v215, v196
	v_add_u32_e32 v38, 0xffffffe0, v38
	v_cmpx_gt_i32_e32 59, v38
	s_nop 3
	s_cbranch_execz .Lmaskx_done_3
	v_mov_b32_e32 v79, v248
	v_cmpx_gt_i32_e32 58, v38
	v_mov_b32_e32 v78, v248
	v_cmpx_gt_i32_e32 57, v38
	v_mov_b32_e32 v77, v248
	v_cmpx_gt_i32_e32 56, v38
	v_mov_b32_e32 v76, v248
	v_cmpx_gt_i32_e32 51, v38
	v_mov_b32_e32 v75, v248
	v_cmpx_gt_i32_e32 50, v38
	v_mov_b32_e32 v74, v248
	v_cmpx_gt_i32_e32 49, v38
	v_mov_b32_e32 v73, v248
	v_cmpx_gt_i32_e32 48, v38
	v_mov_b32_e32 v72, v248
	v_cmpx_gt_i32_e32 43, v38
	v_mov_b32_e32 v71, v248
	v_cmpx_gt_i32_e32 42, v38
	v_mov_b32_e32 v70, v248
	v_cmpx_gt_i32_e32 41, v38
	v_mov_b32_e32 v69, v248
	v_cmpx_gt_i32_e32 40, v38
	v_mov_b32_e32 v68, v248
	v_cmpx_gt_i32_e32 35, v38
	v_mov_b32_e32 v67, v248
	v_cmpx_gt_i32_e32 34, v38
	v_mov_b32_e32 v66, v248
	v_cmpx_gt_i32_e32 33, v38
	v_mov_b32_e32 v65, v248
	v_cmpx_gt_i32_e32 32, v38
	v_mov_b32_e32 v64, v248
	v_cmpx_gt_i32_e32 27, v38
	v_mov_b32_e32 v95, v248
	v_cmpx_gt_i32_e32 26, v38
	v_mov_b32_e32 v94, v248
	v_cmpx_gt_i32_e32 25, v38
	v_mov_b32_e32 v93, v248
	v_cmpx_gt_i32_e32 24, v38
	v_mov_b32_e32 v92, v248
	v_cmpx_gt_i32_e32 19, v38
	v_mov_b32_e32 v91, v248
	v_cmpx_gt_i32_e32 18, v38
	v_mov_b32_e32 v90, v248
	v_cmpx_gt_i32_e32 17, v38
	v_mov_b32_e32 v89, v248
	v_cmpx_gt_i32_e32 16, v38
	v_mov_b32_e32 v88, v248
	v_cmpx_gt_i32_e32 11, v38
	v_mov_b32_e32 v87, v248
	v_cmpx_gt_i32_e32 10, v38
	v_mov_b32_e32 v86, v248
	v_cmpx_gt_i32_e32 9, v38
	v_mov_b32_e32 v85, v248
	v_cmpx_gt_i32_e32 8, v38
	v_mov_b32_e32 v84, v248
	v_cmpx_gt_i32_e32 3, v38
	v_mov_b32_e32 v83, v248
	v_cmpx_gt_i32_e32 2, v38
	v_mov_b32_e32 v82, v248
	v_cmpx_gt_i32_e32 1, v38
	v_mov_b32_e32 v81, v248
	v_cmpx_gt_i32_e32 0, v38
	v_mov_b32_e32 v80, v248

.LBB0_646:
	v_add_u32_e32 v182, s68, v229
	ds_read_b64_tr_b16 v[192:193], v182 offset:24576
	ds_read_b64_tr_b16 v[194:195], v182 offset:25088
	s_waitcnt lgkmcnt(9)
	v_mfma_f32_32x32x16_f16 v[48:63], v[176:179], v[128:131], v[48:63]
	v_add_f32_e32 v132, v80, v81
	v_add_f32_e32 v132, v82, v132
	v_add_f32_e32 v132, v83, v132
	v_add_f32_e32 v132, v84, v132
	v_add_f32_e32 v132, v85, v132
	v_cvt_pk_f16_f32 v144, v80, v81
	v_cvt_pk_f16_f32 v145, v82, v83
	ds_read_b64_tr_b16 v[176:177], v182 offset:28672
	ds_read_b64_tr_b16 v[178:179], v182 offset:29184
	s_waitcnt lgkmcnt(10)
	v_mfma_f32_32x32x16_f16 v[32:47], v[172:175], v[128:131], v[32:47]
	v_add_f32_e32 v80, v86, v132
	v_add_f32_e32 v80, v87, v80
	v_add_f32_e32 v80, v88, v80
	v_add_f32_e32 v80, v89, v80
	v_cvt_pk_f16_f32 v146, v84, v85
	v_cvt_pk_f16_f32 v147, v86, v87
	ds_read_b64_tr_b16 v[188:189], v182 offset:25600
	ds_read_b64_tr_b16 v[190:191], v182 offset:26112
	s_waitcnt lgkmcnt(11)
	v_mfma_f32_32x32x16_f16 v[48:63], v[168:171], v[124:127], v[48:63]
	v_add_f32_e32 v80, v90, v80
	v_add_f32_e32 v80, v91, v80
	v_add_f32_e32 v80, v92, v80
	v_add_f32_e32 v80, v93, v80
	v_cvt_pk_f16_f32 v140, v88, v89
	v_cvt_pk_f16_f32 v141, v90, v91
	ds_read_b64_tr_b16 v[84:85], v182 offset:29696
	ds_read_b64_tr_b16 v[86:87], v182 offset:30208
	s_waitcnt lgkmcnt(12)
	v_mfma_f32_32x32x16_f16 v[32:47], v[164:167], v[124:127], v[32:47]
	v_add_f32_e32 v80, v94, v80
	v_add_f32_e32 v80, v95, v80
	v_add_f32_e32 v80, v64, v80
	v_add_f32_e32 v88, v65, v80
	v_cvt_pk_f16_f32 v142, v92, v93
	v_cvt_pk_f16_f32 v143, v94, v95
	ds_read_b64_tr_b16 v[80:81], v182 offset:26624
	ds_read_b64_tr_b16 v[82:83], v182 offset:27136
	s_waitcnt lgkmcnt(13)
	v_mfma_f32_32x32x16_f16 v[48:63], v[160:163], v[120:123], v[48:63]
	v_add_f32_e32 v88, v66, v88
	v_add_f32_e32 v88, v67, v88
	v_add_f32_e32 v88, v68, v88
	v_add_f32_e32 v88, v69, v88
	v_cvt_pk_f16_f32 v136, v64, v65
	v_cvt_pk_f16_f32 v137, v66, v67
	ds_read_b64_tr_b16 v[184:185], v182 offset:30720
	ds_read_b64_tr_b16 v[186:187], v182 offset:31232
	s_waitcnt lgkmcnt(14)
	v_mfma_f32_32x32x16_f16 v[32:47], v[152:155], v[120:123], v[32:47]
	v_add_f32_e32 v64, v70, v88
	v_add_f32_e32 v64, v71, v64
	v_add_f32_e32 v64, v72, v64
	v_add_f32_e32 v88, v73, v64
	v_cvt_pk_f16_f32 v138, v68, v69
	v_cvt_pk_f16_f32 v139, v70, v71
	ds_read_b64_tr_b16 v[64:65], v182 offset:27648
	ds_read_b64_tr_b16 v[66:67], v182 offset:28160
	s_waitcnt lgkmcnt(14)
	v_mfma_f32_32x32x16_f16 v[48:63], v[156:159], v[116:119], v[48:63]
	v_add_f32_e32 v68, v74, v88
	v_add_f32_e32 v68, v75, v68
	v_add_f32_e32 v68, v76, v68
	v_add_f32_e32 v68, v77, v68
	v_cvt_pk_f16_f32 v132, v72, v73
	v_cvt_pk_f16_f32 v133, v74, v75
	ds_read_b64_tr_b16 v[180:181], v182 offset:31744
	ds_read_b64_tr_b16 v[182:183], v182 offset:32256
	v_mfma_f32_32x32x16_f16 v[32:47], v[148:151], v[116:119], v[32:47]
	v_add_f32_e32 v68, v78, v68
	v_add_f32_e32 v68, v79, v68
	v_cvt_pk_f16_f32 v134, v76, v77
	v_cvt_pk_f16_f32 v135, v78, v79
	s_add_i32 s28, s37, 3
	s_cmp_ge_u32 s28, s36
	s_cselect_b64 s[50:51], -1, 0
	s_and_b64 vcc, exec, s[50:51]
	s_cbranch_vccnz .LBB0_648
	s_add_i32 s28, s11, s90
	s_mov_b32 s40, m0
	s_mov_b32 m0, s28
	s_nop 0
	global_load_lds_dwordx4 v[220:221], off
	s_mov_b32 m0, s40

; __device__ __forceinline__ void cmask(f32x16& p0, f32x16& p1, int jb, int qrel, int hi) {
;     const float NEG = -INFINITY; int kb = 64 * jb + 4 * hi;
; #pragma unroll
;     for (int r = 0; r < 16; ++r) { int kv = kb + (r & 3) + 8 * (r >> 2); if (kv > qrel) p0[r] = NEG; if (kv + 32 > qrel) p1[r] = NEG; }
; }
.LBB0_711:
	v_add_u32_e32 v184, s18, v229
	ds_read_b64_tr_b16 v[180:181], v184 offset:24576
	ds_read_b64_tr_b16 v[182:183], v184 offset:25088
	s_waitcnt lgkmcnt(9)
	v_mfma_f32_32x32x16_f16 v[48:63], v[176:179], v[128:131], v[48:63]
	v_add_f32_e32 v132, v80, v81
	v_add_f32_e32 v132, v82, v132
	v_add_f32_e32 v132, v83, v132
	v_add_f32_e32 v132, v84, v132
	v_add_f32_e32 v132, v85, v132
	v_cvt_pk_f16_f32 v144, v80, v81
	v_cvt_pk_f16_f32 v145, v82, v83
	ds_read_b64_tr_b16 v[80:81], v184 offset:28672
	ds_read_b64_tr_b16 v[82:83], v184 offset:29184
	s_waitcnt lgkmcnt(10)
	v_mfma_f32_32x32x16_f16 v[32:47], v[172:175], v[128:131], v[32:47]
	v_add_f32_e32 v128, v86, v132
	v_add_f32_e32 v128, v87, v128
	v_add_f32_e32 v128, v88, v128
	v_add_f32_e32 v128, v89, v128
	v_cvt_pk_f16_f32 v146, v84, v85
	v_cvt_pk_f16_f32 v147, v86, v87
	ds_read_b64_tr_b16 v[84:85], v184 offset:25600
	ds_read_b64_tr_b16 v[86:87], v184 offset:26112
	s_waitcnt lgkmcnt(11)
	v_mfma_f32_32x32x16_f16 v[48:63], v[168:171], v[124:127], v[48:63]
	v_add_f32_e32 v128, v90, v128
	v_add_f32_e32 v128, v91, v128
	v_add_f32_e32 v128, v92, v128
	v_add_f32_e32 v128, v93, v128
	v_cvt_pk_f16_f32 v140, v88, v89
	v_cvt_pk_f16_f32 v141, v90, v91
	ds_read_b64_tr_b16 v[88:89], v184 offset:29696
	ds_read_b64_tr_b16 v[90:91], v184 offset:30208
	s_waitcnt lgkmcnt(12)
	v_mfma_f32_32x32x16_f16 v[32:47], v[164:167], v[124:127], v[32:47]
	v_add_f32_e32 v124, v94, v128
	v_add_f32_e32 v124, v95, v124
	v_add_f32_e32 v124, v64, v124
	v_add_f32_e32 v124, v65, v124
	v_cvt_pk_f16_f32 v142, v92, v93
	v_cvt_pk_f16_f32 v143, v94, v95
	ds_read_b64_tr_b16 v[92:93], v184 offset:26624
	ds_read_b64_tr_b16 v[94:95], v184 offset:27136
	s_waitcnt lgkmcnt(13)
	v_mfma_f32_32x32x16_f16 v[48:63], v[160:163], v[120:123], v[48:63]
	v_add_f32_e32 v124, v66, v124
	v_add_f32_e32 v124, v67, v124
	v_add_f32_e32 v124, v68, v124
	v_add_f32_e32 v124, v69, v124
	v_cvt_pk_f16_f32 v136, v64, v65
	v_cvt_pk_f16_f32 v137, v66, v67
	ds_read_b64_tr_b16 v[64:65], v184 offset:30720
	ds_read_b64_tr_b16 v[66:67], v184 offset:31232
	s_waitcnt lgkmcnt(14)
	v_mfma_f32_32x32x16_f16 v[32:47], v[152:155], v[120:123], v[32:47]
	v_add_f32_e32 v120, v70, v124
	v_add_f32_e32 v120, v71, v120
	v_add_f32_e32 v120, v72, v120
	v_add_f32_e32 v120, v73, v120
	v_cvt_pk_f16_f32 v138, v68, v69
	v_cvt_pk_f16_f32 v139, v70, v71
	ds_read_b64_tr_b16 v[68:69], v184 offset:27648
	ds_read_b64_tr_b16 v[70:71], v184 offset:28160
	s_waitcnt lgkmcnt(14)
	v_mfma_f32_32x32x16_f16 v[48:63], v[156:159], v[116:119], v[48:63]
	v_add_f32_e32 v120, v74, v120
	v_add_f32_e32 v120, v75, v120
	v_add_f32_e32 v120, v76, v120
	v_add_f32_e32 v120, v77, v120
	v_cvt_pk_f16_f32 v132, v72, v73
	v_cvt_pk_f16_f32 v133, v74, v75
	ds_read_b64_tr_b16 v[72:73], v184 offset:31744
	ds_read_b64_tr_b16 v[74:75], v184 offset:32256
	v_mfma_f32_32x32x16_f16 v[32:47], v[148:151], v[116:119], v[32:47]
	v_add_f32_e32 v116, v78, v120
	v_add_f32_e32 v116, v79, v116
	v_cvt_pk_f16_f32 v134, v76, v77
	v_cvt_pk_f16_f32 v135, v78, v79
	s_andn2_b64 vcc, exec, s[0:1]
	s_cbranch_vccnz .LBB0_713
	s_mov_b64 s[100:101], exec
	v_sub_u32_e32 v77, v215, v231
	v_add_u32_e32 v77, 0xffffff40, v77
	v_cmpx_gt_i32_e32 59, v77
	s_nop 3
	s_cbranch_execz .Lmaskx_done_0
	v_mov_b32_e32 v47, v248
	v_cmpx_gt_i32_e32 58, v77
	v_mov_b32_e32 v46, v248
	v_cmpx_gt_i32_e32 57, v77
	v_mov_b32_e32 v45, v248
	v_cmpx_gt_i32_e32 56, v77
	v_mov_b32_e32 v44, v248
	v_cmpx_gt_i32_e32 51, v77
	v_mov_b32_e32 v43, v248
	v_cmpx_gt_i32_e32 50, v77
	v_mov_b32_e32 v42, v248
	v_cmpx_gt_i32_e32 49, v77
	v_mov_b32_e32 v41, v248
	v_cmpx_gt_i32_e32 48, v77
	v_mov_b32_e32 v40, v248
	v_cmpx_gt_i32_e32 43, v77
	v_mov_b32_e32 v39, v248
	v_cmpx_gt_i32_e32 42, v77
	v_mov_b32_e32 v38, v248
	v_cmpx_gt_i32_e32 41, v77
	v_mov_b32_e32 v37, v248
	v_cmpx_gt_i32_e32 40, v77
	v_mov_b32_e32 v36, v248
	v_cmpx_gt_i32_e32 35, v77
	v_mov_b32_e32 v35, v248
	v_cmpx_gt_i32_e32 34, v77
	v_mov_b32_e32 v34, v248
	v_cmpx_gt_i32_e32 33, v77
	v_mov_b32_e32 v33, v248
	v_cmpx_gt_i32_e32 32, v77
	v_mov_b32_e32 v32, v248
	v_cmpx_gt_i32_e32 27, v77
	v_mov_b32_e32 v63, v248
	v_cmpx_gt_i32_e32 26, v77
	v_mov_b32_e32 v62, v248
	v_cmpx_gt_i32_e32 25, v77
	v_mov_b32_e32 v61, v248
	v_cmpx_gt_i32_e32 24, v77
	v_mov_b32_e32 v60, v248
	v_cmpx_gt_i32_e32 19, v77
	v_mov_b32_e32 v59, v248
	v_cmpx_gt_i32_e32 18, v77
	v_mov_b32_e32 v58, v248
	v_cmpx_gt_i32_e32 17, v77
	v_mov_b32_e32 v57, v248
	v_cmpx_gt_i32_e32 16, v77
	v_mov_b32_e32 v56, v248
	v_cmpx_gt_i32_e32 11, v77
	v_mov_b32_e32 v55, v248
	v_cmpx_gt_i32_e32 10, v77
	v_mov_b32_e32 v54, v248
	v_cmpx_gt_i32_e32 9, v77
	v_mov_b32_e32 v53, v248
	v_cmpx_gt_i32_e32 8, v77
	v_mov_b32_e32 v52, v248
	v_cmpx_gt_i32_e32 3, v77
	v_mov_b32_e32 v51, v248
	v_cmpx_gt_i32_e32 2, v77
	v_mov_b32_e32 v50, v248
	v_cmpx_gt_i32_e32 1, v77
	v_mov_b32_e32 v49, v248
	v_cmpx_gt_i32_e32 0, v77
	v_mov_b32_e32 v48, v248
